# phase-4 sub-LN loop: 2x unrolled with loads two items ahead (counted vmcnt) on top of QK pipelining and P7 epilogue batching
# speedup vs baseline: 1.0224x; 1.0224x over previous
; #define GAS __attribute__((address_space(1)))
; __device__ __forceinline__ f32x4 unpack4(u32x2 w) { return (f32x4){bflo(w.x), bfhi(w.x), bflo(w.y), bfhi(w.y)}; }
; __device__ __forceinline__ void phase4(KP kp, int wave, int bid, int G) {
;     ...
;     const int gw = bid * NWAVES + wave, NGW = G * NWAVES;
;     float lam;
;     { const float* q1 = (const float*)KIN(8); const float* k1 = (const float*)KIN(9); const float* q2 = (const float*)KIN(10); const float* k2 = (const float*)KIN(11);
;       const float s1 = wave_sum(q1[lane] * k1[lane] + q1[lane + 64] * k1[lane + 64]), s2 = wave_sum(q2[lane] * k2[lane] + q2[lane + 64] * k2[lane + 64]);
;       lam = expf(s1) - expf(s2) + 0.2f; }
;     const bf16* OA = (const bf16*)(ws + WS_OA); bf16* ON = (bf16*)(ws + WS_ON);
;     const f32x4 sg = *(const GAS f32x4*)((const float*)KIN(12) + 4 * lane) * 0.8f;
;     for (int it = gw; it < T * 8; it += NGW) { const int t = it >> 3, hd = it & 7;
;         const bf16* o0 = OA + (size_t)t * 4096 + hd * 512 + 4 * lane;
;         const f32x4 d = unpack4(*(const GAS u32x2*)o0) - lam * unpack4(*(const GAS u32x2*)(o0 + 256));
.LBB0_706:
	s_cmp_lt_i32 s84, 5
	s_cselect_b64 s[2:3], -1, 0
	s_cmp_gt_i32 s85, 4
	s_cselect_b64 s[4:5], -1, 0
	s_and_b64 s[2:3], s[2:3], s[4:5]
	s_andn2_b64 vcc, exec, s[2:3]
	s_cbranch_vccnz .LBB0_767
	s_waitcnt lgkmcnt(0)
	s_mov_b64 s[26:27], s[0:1]
	s_waitcnt vmcnt(0)
	v_mbcnt_lo_u32_b32 v0, -1, 0
	v_mbcnt_hi_u32_b32 v0, -1, v0
	s_load_dwordx8 s[8:15], s[26:27], 0x40
	v_ashrrev_i32_e32 v1, 31, v0
	v_lshlrev_b64 v[2:3], 2, v[0:1]
	v_mbcnt_lo_u32_b32 v1, -1, 0
	s_lshl_b32 s2, s81, 3
	s_waitcnt lgkmcnt(0)
	v_lshl_add_u64 v[4:5], s[8:9], 0, v[2:3]
	v_lshl_add_u64 v[6:7], s[10:11], 0, v[2:3]
	global_load_dword v8, v[4:5], off
	global_load_dword v9, v[4:5], off offset:256
	global_load_dword v10, v[6:7], off
	global_load_dword v11, v[6:7], off offset:256
	v_lshl_add_u64 v[4:5], s[12:13], 0, v[2:3]
	v_lshl_add_u64 v[2:3], s[14:15], 0, v[2:3]
	global_load_dword v6, v[2:3], off offset:256
	global_load_dword v7, v[4:5], off offset:256
	global_load_dword v12, v[4:5], off
	global_load_dword v13, v[2:3], off
	v_mbcnt_hi_u32_b32 v3, -1, v1
	v_and_b32_e32 v1, 64, v3
	v_xor_b32_e32 v2, 1, v3
	v_add_u32_e32 v20, 64, v1
	v_cmp_lt_i32_e32 vcc, v2, v20
	v_xor_b32_e32 v4, 2, v3
	v_xor_b32_e32 v5, 4, v3
	v_cndmask_b32_e32 v1, v3, v2, vcc
	v_lshlrev_b32_e32 v1, 2, v1
	v_cmp_lt_i32_e32 vcc, v4, v20
	v_xor_b32_e32 v14, 8, v3
	v_xor_b32_e32 v15, 16, v3
	v_cndmask_b32_e32 v2, v3, v4, vcc
	v_lshlrev_b32_e32 v2, 2, v2
	v_cmp_lt_i32_e32 vcc, v5, v20
	v_xor_b32_e32 v19, 32, v3
	s_load_dwordx2 s[6:7], s[26:27], 0xc8
	v_cndmask_b32_e32 v5, v3, v5, vcc
	v_lshlrev_b32_e32 v16, 2, v5
	v_cmp_lt_i32_e32 vcc, v14, v20
	s_add_i32 s17, s82, s2
	s_lshl_b32 s18, s16, 3
	s_cmp_gt_i32 s17, 0xffff
	s_waitcnt vmcnt(4)
	v_mul_f32_e32 v9, v9, v11
	s_waitcnt vmcnt(2)
	v_mul_f32_e32 v6, v7, v6
	v_fmac_f32_e32 v9, v8, v10
	s_waitcnt vmcnt(0)
	v_fmac_f32_e32 v6, v12, v13
	ds_bpermute_b32 v7, v1, v9
	ds_bpermute_b32 v8, v1, v6
	s_waitcnt lgkmcnt(0)
	v_add_f32_e32 v4, v9, v7
	v_add_f32_e32 v6, v6, v8
	ds_bpermute_b32 v7, v2, v4
	ds_bpermute_b32 v8, v2, v6
	s_waitcnt lgkmcnt(1)
	v_add_f32_e32 v4, v4, v7
	s_waitcnt lgkmcnt(0)
	v_add_f32_e32 v5, v6, v8
	ds_bpermute_b32 v6, v16, v4
	ds_bpermute_b32 v7, v16, v5
	v_cndmask_b32_e32 v8, v3, v14, vcc
	v_lshlrev_b32_e32 v17, 2, v8
	v_cmp_lt_i32_e32 vcc, v15, v20
	s_waitcnt lgkmcnt(1)
	v_add_f32_e32 v4, v4, v6
	s_waitcnt lgkmcnt(0)
	v_add_f32_e32 v5, v5, v7
	ds_bpermute_b32 v6, v17, v4
	ds_bpermute_b32 v7, v17, v5
	v_cndmask_b32_e32 v8, v3, v15, vcc
	v_lshlrev_b32_e32 v18, 2, v8
	v_cmp_lt_i32_e32 vcc, v19, v20
	s_waitcnt lgkmcnt(1)
	v_add_f32_e32 v4, v4, v6
	s_waitcnt lgkmcnt(0)
	v_add_f32_e32 v6, v5, v7
	ds_bpermute_b32 v5, v18, v4
	ds_bpermute_b32 v7, v18, v6
	v_cndmask_b32_e32 v3, v3, v19, vcc
	v_lshlrev_b32_e32 v19, 2, v3
	s_waitcnt lgkmcnt(1)
	v_add_f32_e32 v5, v4, v5
	s_waitcnt lgkmcnt(0)
	v_add_f32_e32 v3, v6, v7
	ds_bpermute_b32 v6, v19, v5
	ds_bpermute_b32 v4, v19, v3
	s_cbranch_scc1 .LBB0_710
	s_load_dwordx2 s[2:3], s[26:27], 0x60
	v_lshlrev_b32_e32 v8, 2, v0
	v_ashrrev_i32_e32 v9, 31, v8
	s_mov_b32 s9, 0x3fb8aa3b
	s_waitcnt lgkmcnt(0)
	v_add_f32_e32 v3, v3, v4
	v_mov_b32_e32 v10, s2
	v_mov_b32_e32 v11, s3
	v_lshl_add_u64 v[10:11], v[8:9], 2, v[10:11]
	global_load_dwordx4 v[22:25], v[10:11], off
	v_add_f32_e32 v10, v5, v6
	v_mul_f32_e32 v4, 0x3fb8aa3b, v10
	v_mul_f32_e32 v5, 0x3fb8aa3b, v3
	v_fma_f32 v12, v10, s9, -v4
	v_rndne_f32_e32 v13, v4
	v_fma_f32 v14, v3, s9, -v5
	v_rndne_f32_e32 v15, v5
	v_fmac_f32_e32 v12, 0x32a5705f, v10
	v_sub_f32_e32 v4, v4, v13
	v_fmac_f32_e32 v14, 0x32a5705f, v3
	v_sub_f32_e32 v5, v5, v15
	v_add_f32_e32 v12, v4, v12
	v_lshlrev_b64 v[6:7], 1, v[8:9]
	v_cvt_i32_f32_e32 v8, v13
	v_add_f32_e32 v13, v5, v14
	v_exp_f32_e32 v12, v12
	v_cvt_i32_f32_e32 v9, v15
	v_exp_f32_e32 v13, v13
	s_mov_b32 s19, 0xc2ce8ed0
	v_ldexp_f32 v8, v12, v8
	v_cmp_ngt_f32_e32 vcc, s19, v10
	s_bfe_u32 s3, s66, 0x30006
	s_mov_b32 s20, 0x42b17218
	v_ldexp_f32 v9, v13, v9
	v_cndmask_b32_e32 v8, 0, v8, vcc
	v_cmp_ngt_f32_e32 vcc, s19, v3
	v_mov_b32_e32 v11, 0x7f800000
	s_lshl_b32 s21, s3, 9
	s_lshl_b32 s3, s3, 10
	v_cndmask_b32_e32 v9, 0, v9, vcc
	v_cmp_nlt_f32_e32 vcc, s20, v10
	s_add_u32 s14, s6, s3
	s_addc_u32 s15, s7, 0
	v_cndmask_b32_e32 v8, v11, v8, vcc
	v_cmp_nlt_f32_e32 vcc, s20, v3
	v_lshl_add_u64 v[4:5], s[14:15], 0, v[6:7]
	s_add_u32 s14, s6, s21
	v_cndmask_b32_e32 v3, v11, v9, vcc
	v_sub_f32_e32 v3, v8, v3
	s_addc_u32 s15, s7, 0
	v_add_f32_e32 v8, 0x3e4ccccd, v3
	s_mov_b32 s2, 0x3f4ccccd
	s_mov_b64 s[10:11], 0x48000000
	s_mov_b64 s[12:13], 0x4c000000
	v_lshl_add_u64 v[6:7], s[14:15], 0, v[6:7]
	v_mov_b32_e32 v10, v8
	s_mov_b32 s4, 0xffff0000
	v_mov_b32_e32 v20, 0x3727c5ac
	s_mov_b32 s5, 0xf800000
	v_mov_b32_e32 v21, 0x260
	s_movk_i32 s8, 0x7fff
	v_lshl_add_u64 v[4:5], v[4:5], 0, s[10:11]
	v_lshl_add_u64 v[6:7], v[6:7], 0, s[12:13]
	v_mov_b32_e32 v9, v8
	v_mov_b32_e32 v3, v8
	v_xor_b32_e32 v10, 0x80000000, v10
	s_mov_b32 s9, s17
	s_waitcnt vmcnt(0)
	v_pk_mul_f32 v[12:13], v[24:25], s[2:3] op_sel_hi:[1,0]
	v_pk_mul_f32 v[14:15], v[22:23], s[2:3] op_sel_hi:[1,0]
	s_ashr_i32 s22, s9, 3
	s_ashr_i32 s23, s22, 31
	s_lshl_b64 s[22:23], s[22:23], 13
	v_lshl_add_u64 v[60:61], v[4:5], 0, s[22:23]
	global_load_dwordx2 v[56:57], v[60:61], off
	global_load_dwordx2 v[58:59], v[60:61], off offset:512
	s_add_i32 s24, s9, s18
	s_min_i32 s24, s24, 0xffff
	s_ashr_i32 s22, s24, 3
	s_ashr_i32 s23, s22, 31
	s_lshl_b64 s[22:23], s[22:23], 13
	v_lshl_add_u64 v[60:61], v[4:5], 0, s[22:23]
	global_load_dwordx2 v[62:63], v[60:61], off
	global_load_dwordx2 v[64:65], v[60:61], off offset:512
	s_waitcnt vmcnt(0)
; #define GAS __attribute__((address_space(1)))
; __device__ __forceinline__ float dot4(f32x4 a, f32x4 b) { return (a.x * b.x + a.y * b.y) + (a.z * b.z + a.w * b.w); }
; __device__ __forceinline__ u32x2 pack4(f32x4 v) { u32x2 w; w.x = pk2(v.x, v.y); w.y = pk2(v.z, v.w); return w; }
; __device__ __forceinline__ f32x4 unpack4(u32x2 w) { return (f32x4){bflo(w.x), bfhi(w.x), bflo(w.y), bfhi(w.y)}; }
; __device__ __forceinline__ void phase4(KP kp, int wave, int bid, int G) {
;     ...
;     for (int it = gw; it < T * 8; it += NGW) { const int t = it >> 3, hd = it & 7;
;         const bf16* o0 = OA + (size_t)t * 4096 + hd * 512 + 4 * lane;
;         const f32x4 d = unpack4(*(const GAS u32x2*)o0) - lam * unpack4(*(const GAS u32x2*)(o0 + 256));
;         const float rstd = 1.0f / sqrtf(wave_sum(dot4(d, d)) * (1.0f / 256.0f) + EPS);
;         *(GAS u32x2*)(ON + (size_t)t * 4096 + hd * 256 + 4 * lane) = pack4(d * rstd * sg); }
.LBB0_709:
	s_ashr_i32 s2, s9, 3
	s_ashr_i32 s3, s2, 31
	s_lshl_b64 s[2:3], s[2:3], 13
	v_xor_b32_e32 v11, 0x80000000, v3
	v_lshl_add_u64 v[22:23], v[6:7], 0, s[2:3]
	s_lshl_b32 s24, s18, 1
	s_add_i32 s24, s24, s9
	s_min_i32 s24, s24, 0xffff
	s_ashr_i32 s22, s24, 3
	s_ashr_i32 s23, s22, 31
	s_lshl_b64 s[22:23], s[22:23], 13
	v_lshl_add_u64 v[60:61], v[4:5], 0, s[22:23]
	s_add_i32 s9, s9, s18
	s_waitcnt vmcnt(4)
	v_lshlrev_b32_e32 v28, 16, v56
	v_and_b32_e32 v29, 0xffff0000, v56
	v_lshlrev_b32_e32 v24, 16, v57
	v_and_b32_e32 v25, 0xffff0000, v57
	v_lshlrev_b32_e32 v30, 16, v58
	v_and_b32_e32 v31, 0xffff0000, v58
	v_lshlrev_b32_e32 v26, 16, v59
	v_and_b32_e32 v27, 0xffff0000, v59
	global_load_dwordx2 v[56:57], v[60:61], off
	global_load_dwordx2 v[58:59], v[60:61], off offset:512
	v_pk_fma_f32 v[28:29], v[8:9], v[30:31], v[28:29] neg_lo:[1,0,0] neg_hi:[1,0,0]
	v_pk_fma_f32 v[24:25], v[10:11], v[26:27], v[24:25]
	v_pk_mul_f32 v[30:31], v[28:29], v[28:29]
	v_pk_mul_f32 v[26:27], v[24:25], v[24:25]
	s_nop 0
	v_pk_mov_b32 v[32:33], v[30:31], v[26:27] op_sel:[1,0]
	v_mov_b32_e32 v31, v27
	v_pk_add_f32 v[26:27], v[32:33], v[30:31]
	s_nop 0
	v_add_f32_e32 v11, v26, v27
	ds_bpermute_b32 v26, v1, v11
	s_waitcnt lgkmcnt(0)
	v_add_f32_e32 v11, v11, v26
	ds_bpermute_b32 v26, v2, v11
	s_waitcnt lgkmcnt(0)
	v_add_f32_e32 v11, v11, v26
	ds_bpermute_b32 v26, v16, v11
	s_waitcnt lgkmcnt(0)
	v_add_f32_e32 v11, v11, v26
	ds_bpermute_b32 v26, v17, v11
	s_waitcnt lgkmcnt(0)
	v_add_f32_e32 v11, v11, v26
	ds_bpermute_b32 v26, v18, v11
	s_waitcnt lgkmcnt(0)
	v_add_f32_e32 v11, v11, v26
	ds_bpermute_b32 v26, v19, v11
	s_waitcnt lgkmcnt(0)
	v_add_f32_e32 v11, v11, v26
	v_fmamk_f32 v11, v11, 0x3b800000, v20
	v_mul_f32_e32 v26, 0x4f800000, v11
	v_cmp_gt_f32_e32 vcc, s5, v11
	s_nop 1
	v_cndmask_b32_e32 v11, v11, v26, vcc
	v_sqrt_f32_e32 v26, v11
	s_nop 0
	v_add_u32_e32 v27, -1, v26
	v_add_u32_e32 v30, 1, v26
	v_fma_f32 v31, -v27, v26, v11
	v_fma_f32 v32, -v30, v26, v11
	v_cmp_ge_f32_e64 s[2:3], 0, v31
	s_nop 1
	v_cndmask_b32_e64 v26, v26, v27, s[2:3]
	v_cmp_lt_f32_e64 s[2:3], 0, v32
	s_nop 1
	v_cndmask_b32_e64 v26, v26, v30, s[2:3]
	v_mul_f32_e32 v27, 0x37800000, v26
	v_cndmask_b32_e32 v26, v26, v27, vcc
	v_cmp_class_f32_e32 vcc, v11, v21
	s_nop 1
	v_cndmask_b32_e32 v11, v26, v11, vcc
	v_div_scale_f32 v26, s[2:3], v11, v11, 1.0
	v_rcp_f32_e32 v30, v26
	v_div_scale_f32 v27, vcc, 1.0, v11, 1.0
	v_fma_f32 v31, -v26, v30, 1.0
	v_fmac_f32_e32 v30, v31, v30
	v_mul_f32_e32 v31, v27, v30
	v_fma_f32 v32, -v26, v31, v27
	v_fmac_f32_e32 v31, v32, v30
	v_fma_f32 v26, -v26, v31, v27
	v_div_fmas_f32 v26, v26, v30, v31
	v_div_fixup_f32 v26, v26, v11, 1.0
	v_pk_mul_f32 v[28:29], v[28:29], v[26:27] op_sel_hi:[1,0]
	v_pk_mul_f32 v[24:25], v[24:25], v[26:27] op_sel_hi:[1,0]
	v_pk_mul_f32 v[26:27], v[14:15], v[28:29]
	v_pk_mul_f32 v[24:25], v[12:13], v[24:25]
	v_bfe_u32 v11, v26, 16, 1
	v_bfe_u32 v29, v24, 16, 1
	v_bfe_u32 v28, v27, 16, 1
	v_bfe_u32 v30, v25, 16, 1
	v_add3_u32 v11, v26, v11, s8
	v_add3_u32 v24, v24, v29, s8
	v_add3_u32 v26, v27, v28, s8
	v_add3_u32 v25, v25, v30, s8
	v_lshrrev_b32_e32 v11, 16, v11
	v_lshrrev_b32_e32 v27, 16, v24
	v_and_or_b32 v24, v26, s4, v11
	v_and_or_b32 v25, v25, s4, v27
	global_store_dwordx2 v[22:23], v[24:25], off
	s_cmp_gt_i32 s9, 0xffff
	s_cbranch_scc1 .Lp4_exit
	s_ashr_i32 s2, s9, 3
	s_ashr_i32 s3, s2, 31
	s_lshl_b64 s[2:3], s[2:3], 13
	v_xor_b32_e32 v11, 0x80000000, v3
	v_lshl_add_u64 v[22:23], v[6:7], 0, s[2:3]
	s_lshl_b32 s24, s18, 1
	s_add_i32 s24, s24, s9
	s_min_i32 s24, s24, 0xffff
	s_ashr_i32 s22, s24, 3
	s_ashr_i32 s23, s22, 31
	s_lshl_b64 s[22:23], s[22:23], 13
	v_lshl_add_u64 v[60:61], v[4:5], 0, s[22:23]
	s_add_i32 s9, s9, s18
	s_waitcnt vmcnt(4)
	v_lshlrev_b32_e32 v28, 16, v62
	v_and_b32_e32 v29, 0xffff0000, v62
	v_lshlrev_b32_e32 v24, 16, v63
	v_and_b32_e32 v25, 0xffff0000, v63
	v_lshlrev_b32_e32 v30, 16, v64
	v_and_b32_e32 v31, 0xffff0000, v64
	v_lshlrev_b32_e32 v26, 16, v65
	v_and_b32_e32 v27, 0xffff0000, v65
	global_load_dwordx2 v[62:63], v[60:61], off
	global_load_dwordx2 v[64:65], v[60:61], off offset:512
	v_pk_fma_f32 v[28:29], v[8:9], v[30:31], v[28:29] neg_lo:[1,0,0] neg_hi:[1,0,0]
	v_pk_fma_f32 v[24:25], v[10:11], v[26:27], v[24:25]
	v_pk_mul_f32 v[30:31], v[28:29], v[28:29]
	v_pk_mul_f32 v[26:27], v[24:25], v[24:25]
	s_nop 0
	v_pk_mov_b32 v[32:33], v[30:31], v[26:27] op_sel:[1,0]
	v_mov_b32_e32 v31, v27
	v_pk_add_f32 v[26:27], v[32:33], v[30:31]
	s_nop 0
	v_add_f32_e32 v11, v26, v27
	ds_bpermute_b32 v26, v1, v11
	s_waitcnt lgkmcnt(0)
	v_add_f32_e32 v11, v11, v26
	ds_bpermute_b32 v26, v2, v11
	s_waitcnt lgkmcnt(0)
	v_add_f32_e32 v11, v11, v26
	ds_bpermute_b32 v26, v16, v11
	s_waitcnt lgkmcnt(0)
	v_add_f32_e32 v11, v11, v26
	ds_bpermute_b32 v26, v17, v11
	s_waitcnt lgkmcnt(0)
	v_add_f32_e32 v11, v11, v26
	ds_bpermute_b32 v26, v18, v11
	s_waitcnt lgkmcnt(0)
	v_add_f32_e32 v11, v11, v26
	ds_bpermute_b32 v26, v19, v11
	s_waitcnt lgkmcnt(0)
	v_add_f32_e32 v11, v11, v26
	v_fmamk_f32 v11, v11, 0x3b800000, v20
	v_mul_f32_e32 v26, 0x4f800000, v11
	v_cmp_gt_f32_e32 vcc, s5, v11
	s_nop 1
	v_cndmask_b32_e32 v11, v11, v26, vcc
	v_sqrt_f32_e32 v26, v11
	s_nop 0
	v_add_u32_e32 v27, -1, v26
	v_add_u32_e32 v30, 1, v26
	v_fma_f32 v31, -v27, v26, v11
	v_fma_f32 v32, -v30, v26, v11
	v_cmp_ge_f32_e64 s[2:3], 0, v31
	s_nop 1
	v_cndmask_b32_e64 v26, v26, v27, s[2:3]
	v_cmp_lt_f32_e64 s[2:3], 0, v32
	s_nop 1
	v_cndmask_b32_e64 v26, v26, v30, s[2:3]
	v_mul_f32_e32 v27, 0x37800000, v26
	v_cndmask_b32_e32 v26, v26, v27, vcc
	v_cmp_class_f32_e32 vcc, v11, v21
	s_nop 1
	v_cndmask_b32_e32 v11, v26, v11, vcc
	v_div_scale_f32 v26, s[2:3], v11, v11, 1.0
	v_rcp_f32_e32 v30, v26
	v_div_scale_f32 v27, vcc, 1.0, v11, 1.0
	v_fma_f32 v31, -v26, v30, 1.0
	v_fmac_f32_e32 v30, v31, v30
	v_mul_f32_e32 v31, v27, v30
	v_fma_f32 v32, -v26, v31, v27
	v_fmac_f32_e32 v31, v32, v30
	v_fma_f32 v26, -v26, v31, v27
	v_div_fmas_f32 v26, v26, v30, v31
	v_div_fixup_f32 v26, v26, v11, 1.0
	v_pk_mul_f32 v[28:29], v[28:29], v[26:27] op_sel_hi:[1,0]
	v_pk_mul_f32 v[24:25], v[24:25], v[26:27] op_sel_hi:[1,0]
	v_pk_mul_f32 v[26:27], v[14:15], v[28:29]
	v_pk_mul_f32 v[24:25], v[12:13], v[24:25]
	v_bfe_u32 v11, v26, 16, 1
	v_bfe_u32 v29, v24, 16, 1
	v_bfe_u32 v28, v27, 16, 1
	v_bfe_u32 v30, v25, 16, 1
	v_add3_u32 v11, v26, v11, s8
	v_add3_u32 v24, v24, v29, s8
	v_add3_u32 v26, v27, v28, s8
	v_add3_u32 v25, v25, v30, s8
	v_lshrrev_b32_e32 v11, 16, v11
	v_lshrrev_b32_e32 v27, 16, v24
	v_and_or_b32 v24, v26, s4, v11
	v_and_or_b32 v25, v25, s4, v27
	global_store_dwordx2 v[22:23], v[24:25], off
	s_cmp_gt_i32 s9, 0xffff
	s_cbranch_scc0 .LBB0_709
; #define GAS __attribute__((address_space(1)))
; __device__ __forceinline__ void phase4(KP kp, int wave, int bid, int G) {
;     ...
;     const bf16* R = (const bf16*)(ws + WS_R); bf16* CV = (bf16*)(ws + WS_ON) + 2048; const float* cw = (const float*)KIN(7);
;     for (int it = gw; it < 2048; it += NGW) { const int tb = it >> 2, ch = (it & 3) * 512 + 8 * lane, t0 = tb * 16;
;         f32x4 w0a = *(const GAS f32x4*)(cw + ch), w0b = *(const GAS f32x4*)(cw + ch + 4), w1a = *(const GAS f32x4*)(cw + 2048 + ch), w1b = *(const GAS f32x4*)(cw + 2048 + ch + 4),
;               w2a = *(const GAS f32x4*)(cw + 4096 + ch), w2b = *(const GAS f32x4*)(cw + 4096 + ch + 4);
.Lp4_exit:
	s_waitcnt vmcnt(0)
.LBB0_710:
	s_cmpk_gt_i32 s17, 0x7ff
	s_cbranch_scc1 .LBB0_717
	s_load_dwordx2 s[8:9], s[26:27], 0x38
	s_add_u32 s5, s6, 0x3e000000
	s_addc_u32 s19, s7, 0
	v_lshlrev_b32_e32 v44, 3, v0
	v_ashrrev_i32_e32 v45, 31, v44
	s_waitcnt lgkmcnt(0)
	s_add_u32 s10, s8, 0x2000
	s_addc_u32 s11, s9, 0
	s_add_u32 s12, s8, 0x4000
	s_addc_u32 s13, s9, 0
	s_lshl_b32 s2, s81, 5
	s_lshl_b32 s3, s82, 2
	s_add_i32 s20, s2, s3
	s_lshl_b32 s2, s81, 12
	s_lshl_b32 s3, s82, 9
	v_lshlrev_b64 v[46:47], 1, v[44:45]
	s_lshl_b32 s21, s16, 5
	s_add_i32 s22, s2, s3
	s_lshl_b32 s23, s16, 12
	v_mov_b32_e32 v0, 0
	s_movk_i32 s24, 0x2000
	s_mov_b32 s25, 0xffff0000
	s_movk_i32 s28, 0x7fff
	s_mov_b32 s29, 0x4c001000
	s_mov_b32 s30, 0x3e006000
	s_mov_b32 s31, 0x3e007000
	s_mov_b32 s34, 0x4c003000
	s_mov_b32 s35, 0x3e00b000
	s_mov_b32 s36, 0x3e00c000
	s_mov_b32 s37, 0x4c005000
	s_mov_b32 s38, 0x3e010000
	s_mov_b32 s39, 0x3e011000
	s_mov_b32 s40, 0x4c007000
